# speedup vs baseline: 1.0002x; 1.0002x over previous
.LBB1_194:
	ds_read_b32 v3, v6
	v_add_u32_e32 v2, 0x400, v2
	v_cmp_lt_u32_e32 vcc, s4, v2
	v_add_u32_e32 v6, 0x1000, v6
	s_or_b64 s[0:1], vcc, s[0:1]
	s_waitcnt lgkmcnt(0)
	global_store_dword v[0:1], v3, off sc1
	v_lshl_add_u64 v[0:1], v[0:1], 0, s[2:3]
	s_andn2_b64 exec, exec, s[0:1]
	s_cbranch_execnz .LBB1_194
